# trimmed redundant ballot re-derivation in top-k bisection loop; replaced 4-op mask select with v_bitop3 in mixer-A softmax
# speedup vs baseline: 1.0054x; 1.0054x over previous
; __device__ __forceinline__ void topk_phase(Frame& F) {
;     ...
;                     const unsigned cand = prefix | (1u << bit); int cnt = 0;
; #pragma unroll
;                     for (int r = 0; r < 24; ++r) if (r < nr) cnt += __popcll(__ballot(cd[r] >= cand));
;                     if (cnt >= 256) { prefix = cand; if (cnt == 256) { exact = true; break; } }
;                 }
.LBB0_958:
	v_lshlrev_b32_e64 v212, v211, 1
	v_or_b32_e32 v212, v212, v210
	s_waitcnt lgkmcnt(11)
	v_cmp_ge_u32_e32 vcc, v0, v212
	s_and_b64 vcc, s[14:15], vcc
	s_and_b64 vcc, vcc, exec
	s_bcnt1_i32_b64 s66, vcc
	v_cmp_ge_u32_e32 vcc, v1, v212
	s_and_b64 vcc, s[16:17], vcc
	s_and_b64 vcc, vcc, exec
	s_bcnt1_i32_b64 s67, vcc
	s_waitcnt lgkmcnt(10)
	v_cmp_ge_u32_e32 vcc, v2, v212
	s_and_b64 vcc, s[18:19], vcc
	s_add_i32 s66, s67, s66
	s_and_b64 vcc, vcc, exec
	s_bcnt1_i32_b64 s67, vcc
	v_cmp_ge_u32_e32 vcc, v3, v212
	s_and_b64 vcc, s[20:21], vcc
	s_add_i32 s66, s66, s67
	s_and_b64 vcc, vcc, exec
	s_bcnt1_i32_b64 s67, vcc
	s_andn2_b64 vcc, exec, s[68:69]
	s_add_i32 s92, s66, s67
	s_cbranch_vccnz .LBB0_978
	s_waitcnt lgkmcnt(9)
	v_cmp_ge_u32_e32 vcc, v4, v212
	s_and_b64 vcc, s[22:23], vcc
	s_and_b64 vcc, vcc, exec
	s_bcnt1_i32_b64 s66, vcc
	s_add_i32 s92, s92, s66
	s_andn2_b64 vcc, exec, s[70:71]
	s_cbranch_vccz .LBB0_979

; __device__ __forceinline__ void topk_phase(Frame& F) {
;     ...
;                     const unsigned cand = prefix | (1u << bit); int cnt = 0;
; #pragma unroll
;                     for (int r = 0; r < 24; ++r) if (r < nr) cnt += __popcll(__ballot(cd[r] >= cand));
;                     if (cnt >= 256) { prefix = cand; if (cnt == 256) { exact = true; break; } }
;                 }
.LBB0_961:
	s_waitcnt lgkmcnt(8)
	v_cmp_ge_u32_e32 vcc, v6, v212
	s_and_b64 vcc, s[26:27], vcc
	s_and_b64 vcc, vcc, exec
	s_bcnt1_i32_b64 s66, vcc
	s_add_i32 s92, s92, s66
	s_andn2_b64 vcc, exec, s[74:75]
	s_cbranch_vccz .LBB0_981

; __device__ __forceinline__ void topk_phase(Frame& F) {
;     ...
;                     const unsigned cand = prefix | (1u << bit); int cnt = 0;
; #pragma unroll
;                     for (int r = 0; r < 24; ++r) if (r < nr) cnt += __popcll(__ballot(cd[r] >= cand));
;                     if (cnt >= 256) { prefix = cand; if (cnt == 256) { exact = true; break; } }
;                 }
.LBB0_963:
	s_waitcnt lgkmcnt(7)
	v_cmp_ge_u32_e32 vcc, v8, v212
	s_and_b64 vcc, s[30:31], vcc
	s_and_b64 vcc, vcc, exec
	s_bcnt1_i32_b64 s66, vcc
	s_add_i32 s92, s92, s66
	s_andn2_b64 vcc, exec, s[78:79]
	s_cbranch_vccz .LBB0_983

; __device__ __forceinline__ void topk_phase(Frame& F) {
;     ...
;                     const unsigned cand = prefix | (1u << bit); int cnt = 0;
; #pragma unroll
;                     for (int r = 0; r < 24; ++r) if (r < nr) cnt += __popcll(__ballot(cd[r] >= cand));
;                     if (cnt >= 256) { prefix = cand; if (cnt == 256) { exact = true; break; } }
;                 }
.LBB0_965:
	s_waitcnt lgkmcnt(6)
	v_cmp_ge_u32_e32 vcc, v10, v212
	s_and_b64 vcc, s[36:37], vcc
	s_and_b64 vcc, vcc, exec
	s_bcnt1_i32_b64 s66, vcc
	s_add_i32 s92, s92, s66
	s_andn2_b64 vcc, exec, s[82:83]
	s_cbranch_vccz .LBB0_985

; __device__ __forceinline__ void topk_phase(Frame& F) {
;     ...
;                     const unsigned cand = prefix | (1u << bit); int cnt = 0;
; #pragma unroll
;                     for (int r = 0; r < 24; ++r) if (r < nr) cnt += __popcll(__ballot(cd[r] >= cand));
;                     if (cnt >= 256) { prefix = cand; if (cnt == 256) { exact = true; break; } }
;                 }
.LBB0_967:
	s_waitcnt lgkmcnt(5)
	v_cmp_ge_u32_e32 vcc, v12, v212
	s_and_b64 vcc, s[40:41], vcc
	s_and_b64 vcc, vcc, exec
	s_bcnt1_i32_b64 s66, vcc
	s_add_i32 s92, s92, s66
	s_andn2_b64 vcc, exec, s[86:87]
	s_cbranch_vccz .LBB0_987

; __device__ __forceinline__ void topk_phase(Frame& F) {
;     ...
;                     const unsigned cand = prefix | (1u << bit); int cnt = 0;
; #pragma unroll
;                     for (int r = 0; r < 24; ++r) if (r < nr) cnt += __popcll(__ballot(cd[r] >= cand));
;                     if (cnt >= 256) { prefix = cand; if (cnt == 256) { exact = true; break; } }
;                 }
.LBB0_969:
	s_waitcnt lgkmcnt(4)
	v_cmp_ge_u32_e32 vcc, v14, v212
	s_and_b64 vcc, s[44:45], vcc
	s_and_b64 vcc, vcc, exec
	s_bcnt1_i32_b64 s66, vcc
	s_add_i32 s92, s92, s66
	s_andn2_b64 vcc, exec, s[90:91]
	s_cbranch_vccz .LBB0_989

; __device__ __forceinline__ void topk_phase(Frame& F) {
;     ...
;                     const unsigned cand = prefix | (1u << bit); int cnt = 0;
; #pragma unroll
;                     for (int r = 0; r < 24; ++r) if (r < nr) cnt += __popcll(__ballot(cd[r] >= cand));
;                     if (cnt >= 256) { prefix = cand; if (cnt == 256) { exact = true; break; } }
;                 }
.LBB0_971:
	s_waitcnt lgkmcnt(3)
	v_cmp_ge_u32_e32 vcc, v16, v212
	s_and_b64 vcc, s[48:49], vcc
	s_and_b64 vcc, vcc, exec
	s_bcnt1_i32_b64 s66, vcc
	s_add_i32 s92, s92, s66
	s_andn2_b64 vcc, exec, s[4:5]
	s_cbranch_vccz .LBB0_991

; __device__ __forceinline__ void topk_phase(Frame& F) {
;     ...
;                     const unsigned cand = prefix | (1u << bit); int cnt = 0;
; #pragma unroll
;                     for (int r = 0; r < 24; ++r) if (r < nr) cnt += __popcll(__ballot(cd[r] >= cand));
;                     if (cnt >= 256) { prefix = cand; if (cnt == 256) { exact = true; break; } }
;                 }
.LBB0_973:
	s_waitcnt lgkmcnt(2)
	v_cmp_ge_u32_e32 vcc, v18, v212
	s_and_b64 vcc, s[52:53], vcc
	s_and_b64 vcc, vcc, exec
	s_bcnt1_i32_b64 s66, vcc
	s_add_i32 s92, s92, s66
	s_andn2_b64 vcc, exec, s[8:9]
	s_cbranch_vccz .LBB0_993

; __device__ __forceinline__ void topk_phase(Frame& F) {
;     ...
;                     const unsigned cand = prefix | (1u << bit); int cnt = 0;
; #pragma unroll
;                     for (int r = 0; r < 24; ++r) if (r < nr) cnt += __popcll(__ballot(cd[r] >= cand));
;                     if (cnt >= 256) { prefix = cand; if (cnt == 256) { exact = true; break; } }
;                 }
.LBB0_975:
	s_waitcnt lgkmcnt(1)
	v_cmp_ge_u32_e32 vcc, v20, v212
	s_and_b64 vcc, s[56:57], vcc
	s_and_b64 vcc, vcc, exec
	s_bcnt1_i32_b64 s66, vcc
	s_add_i32 s92, s92, s66
	s_andn2_b64 vcc, exec, s[12:13]
	s_cbranch_vccz .LBB0_995

; __device__ __forceinline__ void topk_phase(Frame& F) {
;     ...
;                     const unsigned cand = prefix | (1u << bit); int cnt = 0;
; #pragma unroll
;                     for (int r = 0; r < 24; ++r) if (r < nr) cnt += __popcll(__ballot(cd[r] >= cand));
;                     if (cnt >= 256) { prefix = cand; if (cnt == 256) { exact = true; break; } }
;                 }
.LBB0_977:
	s_waitcnt lgkmcnt(0)
	v_cmp_ge_u32_e32 vcc, v22, v212
	s_and_b64 vcc, s[60:61], vcc
	s_and_b64 vcc, vcc, exec
	s_bcnt1_i32_b64 s66, vcc
	s_add_i32 s92, s92, s66
	s_andn2_b64 vcc, exec, s[0:1]
	s_cbranch_vccnz .LBB0_957
	s_branch .LBB0_997

; __device__ __forceinline__ void topk_phase(Frame& F) {
;     ...
;                     const unsigned cand = prefix | (1u << bit); int cnt = 0;
; #pragma unroll
;                     for (int r = 0; r < 24; ++r) if (r < nr) cnt += __popcll(__ballot(cd[r] >= cand));
;                     if (cnt >= 256) { prefix = cand; if (cnt == 256) { exact = true; break; } }
;                 }
.LBB0_979:
	s_waitcnt lgkmcnt(9)
	v_cmp_ge_u32_e32 vcc, v5, v212
	s_and_b64 vcc, s[24:25], vcc
	s_and_b64 vcc, vcc, exec
	s_bcnt1_i32_b64 s66, vcc
	s_add_i32 s92, s92, s66
	s_andn2_b64 vcc, exec, s[72:73]
	s_cbranch_vccz .LBB0_961

; __device__ __forceinline__ void topk_phase(Frame& F) {
;     ...
;                     const unsigned cand = prefix | (1u << bit); int cnt = 0;
; #pragma unroll
;                     for (int r = 0; r < 24; ++r) if (r < nr) cnt += __popcll(__ballot(cd[r] >= cand));
;                     if (cnt >= 256) { prefix = cand; if (cnt == 256) { exact = true; break; } }
;                 }
.LBB0_981:
	s_waitcnt lgkmcnt(8)
	v_cmp_ge_u32_e32 vcc, v7, v212
	s_and_b64 vcc, s[28:29], vcc
	s_and_b64 vcc, vcc, exec
	s_bcnt1_i32_b64 s66, vcc
	s_add_i32 s92, s92, s66
	s_andn2_b64 vcc, exec, s[76:77]
	s_cbranch_vccz .LBB0_963

; __device__ __forceinline__ void topk_phase(Frame& F) {
;     ...
;                     const unsigned cand = prefix | (1u << bit); int cnt = 0;
; #pragma unroll
;                     for (int r = 0; r < 24; ++r) if (r < nr) cnt += __popcll(__ballot(cd[r] >= cand));
;                     if (cnt >= 256) { prefix = cand; if (cnt == 256) { exact = true; break; } }
;                 }
.LBB0_983:
	s_waitcnt lgkmcnt(7)
	v_cmp_ge_u32_e32 vcc, v9, v212
	s_and_b64 vcc, s[34:35], vcc
	s_and_b64 vcc, vcc, exec
	s_bcnt1_i32_b64 s66, vcc
	s_add_i32 s92, s92, s66
	s_andn2_b64 vcc, exec, s[80:81]
	s_cbranch_vccz .LBB0_965

; __device__ __forceinline__ void topk_phase(Frame& F) {
;     ...
;                     const unsigned cand = prefix | (1u << bit); int cnt = 0;
; #pragma unroll
;                     for (int r = 0; r < 24; ++r) if (r < nr) cnt += __popcll(__ballot(cd[r] >= cand));
;                     if (cnt >= 256) { prefix = cand; if (cnt == 256) { exact = true; break; } }
;                 }
.LBB0_985:
	s_waitcnt lgkmcnt(6)
	v_cmp_ge_u32_e32 vcc, v11, v212
	s_and_b64 vcc, s[38:39], vcc
	s_and_b64 vcc, vcc, exec
	s_bcnt1_i32_b64 s66, vcc
	s_add_i32 s92, s92, s66
	s_andn2_b64 vcc, exec, s[84:85]
	s_cbranch_vccz .LBB0_967

; __device__ __forceinline__ void topk_phase(Frame& F) {
;     ...
;                     const unsigned cand = prefix | (1u << bit); int cnt = 0;
; #pragma unroll
;                     for (int r = 0; r < 24; ++r) if (r < nr) cnt += __popcll(__ballot(cd[r] >= cand));
;                     if (cnt >= 256) { prefix = cand; if (cnt == 256) { exact = true; break; } }
;                 }
.LBB0_987:
	s_waitcnt lgkmcnt(5)
	v_cmp_ge_u32_e32 vcc, v13, v212
	s_and_b64 vcc, s[42:43], vcc
	s_and_b64 vcc, vcc, exec
	s_bcnt1_i32_b64 s66, vcc
	s_add_i32 s92, s92, s66
	s_andn2_b64 vcc, exec, s[88:89]
	s_cbranch_vccz .LBB0_969

; __device__ __forceinline__ void topk_phase(Frame& F) {
;     ...
;                     const unsigned cand = prefix | (1u << bit); int cnt = 0;
; #pragma unroll
;                     for (int r = 0; r < 24; ++r) if (r < nr) cnt += __popcll(__ballot(cd[r] >= cand));
;                     if (cnt >= 256) { prefix = cand; if (cnt == 256) { exact = true; break; } }
;                 }
.LBB0_989:
	s_waitcnt lgkmcnt(4)
	v_cmp_ge_u32_e32 vcc, v15, v212
	s_and_b64 vcc, s[46:47], vcc
	s_and_b64 vcc, vcc, exec
	s_bcnt1_i32_b64 s66, vcc
	s_add_i32 s92, s92, s66
	s_andn2_b64 vcc, exec, s[96:97]
	s_cbranch_vccz .LBB0_971

; __device__ __forceinline__ void topk_phase(Frame& F) {
;     ...
;                     const unsigned cand = prefix | (1u << bit); int cnt = 0;
; #pragma unroll
;                     for (int r = 0; r < 24; ++r) if (r < nr) cnt += __popcll(__ballot(cd[r] >= cand));
;                     if (cnt >= 256) { prefix = cand; if (cnt == 256) { exact = true; break; } }
;                 }
.LBB0_991:
	s_waitcnt lgkmcnt(3)
	v_cmp_ge_u32_e32 vcc, v17, v212
	s_and_b64 vcc, s[50:51], vcc
	s_and_b64 vcc, vcc, exec
	s_bcnt1_i32_b64 s66, vcc
	s_add_i32 s92, s92, s66
	s_andn2_b64 vcc, exec, s[6:7]
	s_cbranch_vccz .LBB0_973

; __device__ __forceinline__ void topk_phase(Frame& F) {
;     ...
;                     const unsigned cand = prefix | (1u << bit); int cnt = 0;
; #pragma unroll
;                     for (int r = 0; r < 24; ++r) if (r < nr) cnt += __popcll(__ballot(cd[r] >= cand));
;                     if (cnt >= 256) { prefix = cand; if (cnt == 256) { exact = true; break; } }
;                 }
.LBB0_993:
	s_waitcnt lgkmcnt(2)
	v_cmp_ge_u32_e32 vcc, v19, v212
	s_and_b64 vcc, s[54:55], vcc
	s_and_b64 vcc, vcc, exec
	s_bcnt1_i32_b64 s66, vcc
	s_add_i32 s92, s92, s66
	s_andn2_b64 vcc, exec, s[10:11]
	s_cbranch_vccz .LBB0_975

; __device__ __forceinline__ void topk_phase(Frame& F) {
;     ...
;                     const unsigned cand = prefix | (1u << bit); int cnt = 0;
; #pragma unroll
;                     for (int r = 0; r < 24; ++r) if (r < nr) cnt += __popcll(__ballot(cd[r] >= cand));
;                     if (cnt >= 256) { prefix = cand; if (cnt == 256) { exact = true; break; } }
;                 }
.LBB0_995:
	s_waitcnt lgkmcnt(1)
	v_cmp_ge_u32_e32 vcc, v21, v212
	s_and_b64 vcc, s[58:59], vcc
	s_and_b64 vcc, vcc, exec
	s_bcnt1_i32_b64 s66, vcc
	s_add_i32 s92, s92, s66
	s_andn2_b64 vcc, exec, s[2:3]
	s_cbranch_vccz .LBB0_977

; __device__ __forceinline__ void topk_phase(Frame& F) {
;     ...
;                     const unsigned cand = prefix | (1u << bit); int cnt = 0;
; #pragma unroll
;                     for (int r = 0; r < 24; ++r) if (r < nr) cnt += __popcll(__ballot(cd[r] >= cand));
;                     if (cnt >= 256) { prefix = cand; if (cnt == 256) { exact = true; break; } }
;                 }
.LBB0_997:
	s_waitcnt lgkmcnt(0)
	v_cmp_ge_u32_e32 vcc, v23, v212
	s_and_b64 vcc, s[62:63], vcc
	s_and_b64 vcc, vcc, exec
	s_bcnt1_i32_b64 s66, vcc
	s_add_i32 s92, s92, s66
	s_branch .LBB0_957

; __device__ __forceinline__ void mask_bits(f32x16& p0, f32x16& p1, unsigned long long w, int hi) {
;     const unsigned long long wsft = w >> (4 * hi); const int lo = (int)(unsigned)wsft, hb = (int)(unsigned)(wsft >> 32); const int NEGB = (int)0xFF800000u;
; #pragma unroll
;     for (int r = 0; r < 16; ++r) { const int c = (r & 3) + 8 * (r >> 2);
;         const int t0 = __builtin_amdgcn_sbfe(lo, c, 1), t1 = __builtin_amdgcn_sbfe(hb, c, 1);
;         p0[r] = __int_as_float((__float_as_int(p0[r]) & t0) | (~t0 & NEGB)); p1[r] = __int_as_float((__float_as_int(p1[r]) & t1) | (~t1 & NEGB)); }
; }
; __device__ __forceinline__ void partialSM(f32x16& p0, f32x16& p1, float& m_reg, float& mn, float& alpha) {
;     float pmax = p0[0];
; #pragma unroll
;     for (int r = 1; r < 16; ++r) pmax = fmaxf(pmax, p0[r]);
; #pragma unroll
;     for (int r = 0; r < 16; ++r) pmax = fmaxf(pmax, p1[r]);
;     { auto rr = __builtin_amdgcn_permlane32_swap(__float_as_uint(pmax), __float_as_uint(pmax), false, false);
;       pmax = fmaxf(__uint_as_float(rr[0]), __uint_as_float(rr[1])); }
;     constexpr float C2 = 1.4426950408889634f * SCALE;
;     if (__builtin_expect(__all((pmax - m_reg) * SCALE <= THR), 1)) { mn = m_reg; alpha = 1.f; }
;     else { mn = fmaxf(m_reg, pmax); alpha = __builtin_amdgcn_exp2f((m_reg - mn) * C2); m_reg = mn; }
; template <int VB>
; __device__ __forceinline__ void pv_tile(f32x16* o, int vb0, bf16x8 pa0, bf16x8 pa1, bf16x8 pa2, bf16x8 pa3) {
;     ...
;     PV_D0(0); PV_D0(1); PV_D0(2); PV_D0(3);
.LBB0_1454:
	ds_read_b64_tr_b16 v[170:171], v178 offset:0x4000
	ds_read_b64_tr_b16 v[172:173], v178 offset:0x4800
	ds_read_b64_tr_b16 v[198:199], v178 offset:0x5000
	ds_read_b64_tr_b16 v[200:201], v178 offset:0x5800
	ds_read_b64_tr_b16 v[202:203], v178 offset:0x6000
	ds_read_b64_tr_b16 v[204:205], v178 offset:0x6800
	ds_read_b64_tr_b16 v[206:207], v178 offset:0x7000
	ds_read_b64_tr_b16 v[208:209], v178 offset:0x7800
	s_waitcnt lgkmcnt(0)
	s_nop 0
	v_mfma_f32_32x32x16_bf16 v[2:17], v[146:149], v[170:173], v[2:17]
	ds_read_b64_tr_b16 v[170:171], v178 offset:0x4200
	ds_read_b64_tr_b16 v[172:173], v178 offset:0x4a00
	v_mfma_f32_32x32x16_bf16 v[2:17], v[150:153], v[198:201], v[2:17]
	ds_read_b64_tr_b16 v[198:199], v178 offset:0x5200
	ds_read_b64_tr_b16 v[200:201], v178 offset:0x5a00
	v_mfma_f32_32x32x16_bf16 v[2:17], v[154:157], v[202:205], v[2:17]
	ds_read_b64_tr_b16 v[202:203], v178 offset:0x6200
	ds_read_b64_tr_b16 v[204:205], v178 offset:0x6a00
	v_mfma_f32_32x32x16_bf16 v[2:17], v[158:161], v[206:209], v[2:17]
	ds_read_b64_tr_b16 v[206:207], v178 offset:0x7200
	ds_read_b64_tr_b16 v[208:209], v178 offset:0x7a00
	s_waitcnt lgkmcnt(0)
	v_mfma_f32_32x32x16_bf16 v[50:65], v[146:149], v[170:173], v[50:65]
	ds_read_b64_tr_b16 v[170:171], v178 offset:0x4400
	ds_read_b64_tr_b16 v[172:173], v178 offset:0x4c00
	v_mfma_f32_32x32x16_bf16 v[50:65], v[150:153], v[198:201], v[50:65]
	ds_read_b64_tr_b16 v[198:199], v178 offset:0x5400
	ds_read_b64_tr_b16 v[200:201], v178 offset:0x5c00
	v_mfma_f32_32x32x16_bf16 v[50:65], v[154:157], v[202:205], v[50:65]
	ds_read_b64_tr_b16 v[202:203], v178 offset:0x6400
	ds_read_b64_tr_b16 v[204:205], v178 offset:0x6c00
	v_mfma_f32_32x32x16_bf16 v[50:65], v[158:161], v[206:209], v[50:65]
	ds_read_b64_tr_b16 v[206:207], v178 offset:0x7400
	ds_read_b64_tr_b16 v[208:209], v178 offset:0x7c00
	s_waitcnt lgkmcnt(0)
	v_mfma_f32_32x32x16_bf16 v[34:49], v[146:149], v[170:173], v[34:49]
	ds_read_b64_tr_b16 v[170:171], v178 offset:0x4600
	ds_read_b64_tr_b16 v[172:173], v178 offset:0x4e00
	v_mfma_f32_32x32x16_bf16 v[34:49], v[150:153], v[198:201], v[34:49]
	ds_read_b64_tr_b16 v[198:199], v178 offset:0x5600
	ds_read_b64_tr_b16 v[200:201], v178 offset:0x5e00
	v_mfma_f32_32x32x16_bf16 v[34:49], v[154:157], v[202:205], v[34:49]
	ds_read_b64_tr_b16 v[202:203], v178 offset:0x6600
	ds_read_b64_tr_b16 v[204:205], v178 offset:0x6e00
	v_mfma_f32_32x32x16_bf16 v[34:49], v[158:161], v[206:209], v[34:49]
	ds_read_b64_tr_b16 v[206:207], v178 offset:0x7600
	ds_read_b64_tr_b16 v[208:209], v178 offset:0x7e00
	s_waitcnt lgkmcnt(0)
	v_mfma_f32_32x32x16_bf16 v[18:33], v[146:149], v[170:173], v[18:33]
	s_barrier
	v_mfma_f32_32x32x16_bf16 v[18:33], v[150:153], v[198:201], v[18:33]
	s_waitcnt vmcnt(4)
	v_lshrrev_b64 v[150:151], v166, v[174:175]
	v_bfe_i32 v146, v150, 0, 1
	v_bitop3_b32 v146, v82, s91, v146 bitop3:0xe4
	v_bfe_i32 v82, v150, 1, 1
	v_bitop3_b32 v147, v83, s91, v82 bitop3:0xe4
	v_bfe_i32 v82, v150, 2, 1
	v_bitop3_b32 v148, v84, s91, v82 bitop3:0xe4
	v_bfe_i32 v82, v150, 3, 1
	v_bitop3_b32 v85, v85, s91, v82 bitop3:0xe4
	v_bfe_i32 v82, v150, 8, 1
	v_bitop3_b32 v86, v86, s91, v82 bitop3:0xe4
	v_bfe_i32 v82, v150, 9, 1
	v_bitop3_b32 v87, v87, s91, v82 bitop3:0xe4
	v_bfe_i32 v82, v150, 10, 1
	v_bitop3_b32 v88, v88, s91, v82 bitop3:0xe4
	v_bfe_i32 v82, v150, 11, 1
	v_bitop3_b32 v89, v89, s91, v82 bitop3:0xe4
	v_bfe_i32 v82, v150, 16, 1
	v_bitop3_b32 v90, v90, s91, v82 bitop3:0xe4
	v_bfe_i32 v82, v150, 17, 1
	v_bitop3_b32 v91, v91, s91, v82 bitop3:0xe4
	v_bfe_i32 v82, v150, 18, 1
	v_bitop3_b32 v92, v92, s91, v82 bitop3:0xe4
	v_bfe_i32 v82, v150, 19, 1
	v_bitop3_b32 v93, v93, s91, v82 bitop3:0xe4
	v_bfe_i32 v82, v150, 24, 1
	v_bitop3_b32 v94, v94, s91, v82 bitop3:0xe4
	v_bfe_i32 v82, v150, 25, 1
	v_bitop3_b32 v95, v95, s91, v82 bitop3:0xe4
	v_bfe_i32 v82, v150, 26, 1
	v_bitop3_b32 v149, v96, s91, v82 bitop3:0xe4
	v_bfe_i32 v82, v150, 27, 1
	v_bfe_i32 v152, v151, 0, 1
	v_bfe_i32 v153, v151, 1, 1
	v_bitop3_b32 v96, v97, s91, v82 bitop3:0xe4
	v_max_f32_e32 v82, v147, v147
	v_max_f32_e32 v83, v146, v146
	v_max_f32_e32 v82, v83, v82
	v_bitop3_b32 v67, v67, s91, v153 bitop3:0xe4
	v_bitop3_b32 v66, v66, s91, v152 bitop3:0xe4
	v_max3_f32 v82, v82, v148, v85
	v_bfe_i32 v83, v151, 3, 1
	v_bfe_i32 v84, v151, 2, 1
	v_max3_f32 v82, v82, v86, v87
	v_max3_f32 v82, v82, v88, v89
	v_bitop3_b32 v69, v69, s91, v83 bitop3:0xe4
	v_bitop3_b32 v68, v68, s91, v84 bitop3:0xe4
	v_max3_f32 v82, v82, v90, v91
	v_bfe_i32 v83, v151, 9, 1
	v_bfe_i32 v84, v151, 8, 1
	v_max3_f32 v82, v82, v92, v93
	v_max3_f32 v82, v82, v94, v95
	v_bitop3_b32 v71, v71, s91, v83 bitop3:0xe4
	v_bitop3_b32 v70, v70, s91, v84 bitop3:0xe4
	v_max3_f32 v82, v82, v149, v96
	v_bfe_i32 v83, v151, 11, 1
	v_bfe_i32 v84, v151, 10, 1
	v_max3_f32 v82, v82, v66, v67
	v_max3_f32 v82, v82, v68, v69
	v_bitop3_b32 v73, v73, s91, v83 bitop3:0xe4
	v_bitop3_b32 v72, v72, s91, v84 bitop3:0xe4
	v_max3_f32 v82, v82, v70, v71
	v_max3_f32 v84, v82, v72, v73
	v_bfe_i32 v82, v151, 17, 1
	v_bfe_i32 v83, v151, 16, 1
	v_bitop3_b32 v75, v75, s91, v82 bitop3:0xe4
	v_bitop3_b32 v74, v74, s91, v83 bitop3:0xe4
	v_mov_b32_e32 v83, v75
	v_mov_b32_e32 v82, v74
	v_bfe_i32 v74, v151, 19, 1
	v_bfe_i32 v75, v151, 18, 1
	v_bitop3_b32 v74, v77, s91, v74 bitop3:0xe4
	v_bitop3_b32 v76, v76, s91, v75 bitop3:0xe4
	v_mov_b32_e32 v75, v74
	v_mov_b32_e32 v74, v76
	v_bfe_i32 v76, v151, 25, 1
	v_bfe_i32 v77, v151, 24, 1
	v_mfma_f32_32x32x16_bf16 v[18:33], v[154:157], v[202:205], v[18:33]
	v_bitop3_b32 v76, v79, s91, v76 bitop3:0xe4
	v_bitop3_b32 v78, v78, s91, v77 bitop3:0xe4
	v_mov_b32_e32 v77, v76
	v_mov_b32_e32 v76, v78
	v_bfe_i32 v78, v151, 27, 1
	v_bfe_i32 v79, v151, 26, 1
	v_max3_f32 v84, v84, v82, v83
	v_max3_f32 v84, v84, v74, v75
	v_bitop3_b32 v78, v81, s91, v78 bitop3:0xe4
	v_bitop3_b32 v80, v80, s91, v79 bitop3:0xe4
	v_max3_f32 v84, v84, v76, v77
	v_mov_b32_e32 v79, v78
	v_mov_b32_e32 v78, v80
	v_max3_f32 v80, v84, v78, v79
	v_mov_b32_e32 v81, v80
	v_mfma_f32_32x32x16_bf16 v[18:33], v[158:161], v[206:209], v[18:33]
	s_nop 0
	v_permlane32_swap_b32_e32 v80, v81
	v_max_f32_e32 v81, v81, v81
	v_max_f32_e32 v80, v80, v80
	v_max_f32_e32 v80, v80, v81
	v_sub_f32_e32 v81, v80, v193
	v_mul_f32_e32 v81, 0x3db504f3, v81
	v_cmp_ge_f32_e32 vcc, s92, v81
	s_cmp_eq_u64 vcc, exec
	s_cselect_b64 s[2:3], -1, 0
	s_andn2_b64 vcc, exec, s[24:25]
	s_cbranch_vccnz .LBB0_1456
	s_waitcnt vmcnt(0)
	ds_write_b128 v181, v[130:133] offset:16384
	ds_write_b128 v181, v[134:137] offset:24576
	ds_write_b128 v187, v[138:141] offset:49152
	ds_write_b128 v187, v[142:145] offset:57344

; __device__ __forceinline__ void mask_bits(f32x16& p0, f32x16& p1, unsigned long long w, int hi) {
;     const unsigned long long wsft = w >> (4 * hi); const int lo = (int)(unsigned)wsft, hb = (int)(unsigned)(wsft >> 32); const int NEGB = (int)0xFF800000u;
; #pragma unroll
;     for (int r = 0; r < 16; ++r) { const int c = (r & 3) + 8 * (r >> 2);
;         const int t0 = __builtin_amdgcn_sbfe(lo, c, 1), t1 = __builtin_amdgcn_sbfe(hb, c, 1);
;         p0[r] = __int_as_float((__float_as_int(p0[r]) & t0) | (~t0 & NEGB)); p1[r] = __int_as_float((__float_as_int(p1[r]) & t1) | (~t1 & NEGB)); }
; }
; __device__ __forceinline__ void partialSM(f32x16& p0, f32x16& p1, float& m_reg, float& mn, float& alpha) {
;     float pmax = p0[0];
; #pragma unroll
;     for (int r = 1; r < 16; ++r) pmax = fmaxf(pmax, p0[r]);
; #pragma unroll
;     for (int r = 0; r < 16; ++r) pmax = fmaxf(pmax, p1[r]);
;     { auto rr = __builtin_amdgcn_permlane32_swap(__float_as_uint(pmax), __float_as_uint(pmax), false, false);
;       pmax = fmaxf(__uint_as_float(rr[0]), __uint_as_float(rr[1])); }
;     constexpr float C2 = 1.4426950408889634f * SCALE;
;     if (__builtin_expect(__all((pmax - m_reg) * SCALE <= THR), 1)) { mn = m_reg; alpha = 1.f; }
;     else { mn = fmaxf(m_reg, pmax); alpha = __builtin_amdgcn_exp2f((m_reg - mn) * C2); m_reg = mn; }
; template <int VB>
; __device__ __forceinline__ void pv_tile(f32x16* o, int vb0, bf16x8 pa0, bf16x8 pa1, bf16x8 pa2, bf16x8 pa3) {
;     ...
;     PV_D0(0); PV_D0(1); PV_D0(2); PV_D0(3);
.LBB0_1599:
	ds_read_b64_tr_b16 v[170:171], v178 offset:0x4000
	ds_read_b64_tr_b16 v[172:173], v178 offset:0x4800
	ds_read_b64_tr_b16 v[198:199], v178 offset:0x5000
	ds_read_b64_tr_b16 v[200:201], v178 offset:0x5800
	ds_read_b64_tr_b16 v[202:203], v178 offset:0x6000
	ds_read_b64_tr_b16 v[204:205], v178 offset:0x6800
	ds_read_b64_tr_b16 v[206:207], v178 offset:0x7000
	ds_read_b64_tr_b16 v[208:209], v178 offset:0x7800
	s_waitcnt lgkmcnt(0)
	s_nop 0
	v_mfma_f32_32x32x16_bf16 v[2:17], v[146:149], v[170:173], v[2:17]
	ds_read_b64_tr_b16 v[170:171], v178 offset:0x4200
	ds_read_b64_tr_b16 v[172:173], v178 offset:0x4a00
	v_mfma_f32_32x32x16_bf16 v[2:17], v[150:153], v[198:201], v[2:17]
	ds_read_b64_tr_b16 v[198:199], v178 offset:0x5200
	ds_read_b64_tr_b16 v[200:201], v178 offset:0x5a00
	v_mfma_f32_32x32x16_bf16 v[2:17], v[154:157], v[202:205], v[2:17]
	ds_read_b64_tr_b16 v[202:203], v178 offset:0x6200
	ds_read_b64_tr_b16 v[204:205], v178 offset:0x6a00
	v_mfma_f32_32x32x16_bf16 v[2:17], v[158:161], v[206:209], v[2:17]
	ds_read_b64_tr_b16 v[206:207], v178 offset:0x7200
	ds_read_b64_tr_b16 v[208:209], v178 offset:0x7a00
	s_waitcnt lgkmcnt(0)
	v_mfma_f32_32x32x16_bf16 v[50:65], v[146:149], v[170:173], v[50:65]
	ds_read_b64_tr_b16 v[170:171], v178 offset:0x4400
	ds_read_b64_tr_b16 v[172:173], v178 offset:0x4c00
	v_mfma_f32_32x32x16_bf16 v[50:65], v[150:153], v[198:201], v[50:65]
	ds_read_b64_tr_b16 v[198:199], v178 offset:0x5400
	ds_read_b64_tr_b16 v[200:201], v178 offset:0x5c00
	v_mfma_f32_32x32x16_bf16 v[50:65], v[154:157], v[202:205], v[50:65]
	ds_read_b64_tr_b16 v[202:203], v178 offset:0x6400
	ds_read_b64_tr_b16 v[204:205], v178 offset:0x6c00
	v_mfma_f32_32x32x16_bf16 v[50:65], v[158:161], v[206:209], v[50:65]
	ds_read_b64_tr_b16 v[206:207], v178 offset:0x7400
	ds_read_b64_tr_b16 v[208:209], v178 offset:0x7c00
	s_waitcnt lgkmcnt(0)
	v_mfma_f32_32x32x16_bf16 v[34:49], v[146:149], v[170:173], v[34:49]
	ds_read_b64_tr_b16 v[170:171], v178 offset:0x4600
	ds_read_b64_tr_b16 v[172:173], v178 offset:0x4e00
	v_mfma_f32_32x32x16_bf16 v[34:49], v[150:153], v[198:201], v[34:49]
	ds_read_b64_tr_b16 v[198:199], v178 offset:0x5600
	ds_read_b64_tr_b16 v[200:201], v178 offset:0x5e00
	v_mfma_f32_32x32x16_bf16 v[34:49], v[154:157], v[202:205], v[34:49]
	ds_read_b64_tr_b16 v[202:203], v178 offset:0x6600
	ds_read_b64_tr_b16 v[204:205], v178 offset:0x6e00
	v_mfma_f32_32x32x16_bf16 v[34:49], v[158:161], v[206:209], v[34:49]
	ds_read_b64_tr_b16 v[206:207], v178 offset:0x7600
	ds_read_b64_tr_b16 v[208:209], v178 offset:0x7e00
	s_waitcnt lgkmcnt(0)
	v_mfma_f32_32x32x16_bf16 v[18:33], v[146:149], v[170:173], v[18:33]
	s_barrier
	v_mfma_f32_32x32x16_bf16 v[18:33], v[150:153], v[198:201], v[18:33]
	s_waitcnt vmcnt(4)
	v_lshrrev_b64 v[150:151], v166, v[174:175]
	v_bfe_i32 v146, v150, 0, 1
	v_bitop3_b32 v146, v82, s91, v146 bitop3:0xe4
	v_bfe_i32 v82, v150, 1, 1
	v_bitop3_b32 v147, v83, s91, v82 bitop3:0xe4
	v_bfe_i32 v82, v150, 2, 1
	v_bitop3_b32 v84, v84, s91, v82 bitop3:0xe4
	v_bfe_i32 v82, v150, 3, 1
	v_bitop3_b32 v85, v85, s91, v82 bitop3:0xe4
	v_bfe_i32 v82, v150, 8, 1
	v_bitop3_b32 v86, v86, s91, v82 bitop3:0xe4
	v_bfe_i32 v82, v150, 9, 1
	v_bitop3_b32 v87, v87, s91, v82 bitop3:0xe4
	v_bfe_i32 v82, v150, 10, 1
	v_bitop3_b32 v88, v88, s91, v82 bitop3:0xe4
	v_bfe_i32 v82, v150, 11, 1
	v_bitop3_b32 v89, v89, s91, v82 bitop3:0xe4
	v_bfe_i32 v82, v150, 16, 1
	v_bitop3_b32 v90, v90, s91, v82 bitop3:0xe4
	v_bfe_i32 v82, v150, 17, 1
	v_bitop3_b32 v91, v91, s91, v82 bitop3:0xe4
	v_bfe_i32 v82, v150, 18, 1
	v_bitop3_b32 v92, v92, s91, v82 bitop3:0xe4
	v_bfe_i32 v82, v150, 19, 1
	v_bitop3_b32 v93, v93, s91, v82 bitop3:0xe4
	v_bfe_i32 v82, v150, 24, 1
	v_bitop3_b32 v94, v94, s91, v82 bitop3:0xe4
	v_bfe_i32 v82, v150, 25, 1
	v_bitop3_b32 v95, v95, s91, v82 bitop3:0xe4
	v_bfe_i32 v82, v150, 26, 1
	v_bitop3_b32 v148, v96, s91, v82 bitop3:0xe4
	v_bfe_i32 v82, v150, 27, 1
	v_bfe_i32 v149, v151, 0, 1
	v_bfe_i32 v152, v151, 1, 1
	v_bitop3_b32 v96, v97, s91, v82 bitop3:0xe4
	v_max_f32_e32 v82, v147, v147
	v_max_f32_e32 v83, v146, v146
	v_max_f32_e32 v82, v83, v82
	v_bitop3_b32 v67, v67, s91, v152 bitop3:0xe4
	v_bitop3_b32 v66, v66, s91, v149 bitop3:0xe4
	v_max3_f32 v82, v82, v84, v85
	v_bfe_i32 v83, v151, 3, 1
	v_bfe_i32 v97, v151, 2, 1
	v_max3_f32 v82, v82, v86, v87
	v_max3_f32 v82, v82, v88, v89
	v_bitop3_b32 v69, v69, s91, v83 bitop3:0xe4
	v_bitop3_b32 v68, v68, s91, v97 bitop3:0xe4
	v_max3_f32 v82, v82, v90, v91
	v_bfe_i32 v83, v151, 9, 1
	v_bfe_i32 v97, v151, 8, 1
	v_max3_f32 v82, v82, v92, v93
	v_max3_f32 v82, v82, v94, v95
	v_bitop3_b32 v71, v71, s91, v83 bitop3:0xe4
	v_bitop3_b32 v70, v70, s91, v97 bitop3:0xe4
	v_max3_f32 v82, v82, v148, v96
	v_bfe_i32 v83, v151, 11, 1
	v_bfe_i32 v97, v151, 10, 1
	v_max3_f32 v82, v82, v66, v67
	v_max3_f32 v82, v82, v68, v69
	v_bitop3_b32 v73, v73, s91, v83 bitop3:0xe4
	v_bitop3_b32 v72, v72, s91, v97 bitop3:0xe4
	v_max3_f32 v82, v82, v70, v71
	v_max3_f32 v97, v82, v72, v73
	v_bfe_i32 v82, v151, 17, 1
	v_bfe_i32 v83, v151, 16, 1
	v_bitop3_b32 v75, v75, s91, v82 bitop3:0xe4
	v_bitop3_b32 v74, v74, s91, v83 bitop3:0xe4
	v_mov_b32_e32 v83, v75
	v_mov_b32_e32 v82, v74
	v_bfe_i32 v74, v151, 19, 1
	v_bfe_i32 v75, v151, 18, 1
	v_bitop3_b32 v74, v77, s91, v74 bitop3:0xe4
	v_bitop3_b32 v76, v76, s91, v75 bitop3:0xe4
	v_mov_b32_e32 v75, v74
	v_mov_b32_e32 v74, v76
	v_bfe_i32 v76, v151, 25, 1
	v_bfe_i32 v77, v151, 24, 1
	v_mfma_f32_32x32x16_bf16 v[18:33], v[154:157], v[202:205], v[18:33]
	v_bitop3_b32 v76, v79, s91, v76 bitop3:0xe4
	v_bitop3_b32 v78, v78, s91, v77 bitop3:0xe4
	v_mov_b32_e32 v77, v76
	v_mov_b32_e32 v76, v78
	v_bfe_i32 v78, v151, 27, 1
	v_bfe_i32 v79, v151, 26, 1
	v_max3_f32 v97, v97, v82, v83
	v_max3_f32 v97, v97, v74, v75
	v_bitop3_b32 v78, v81, s91, v78 bitop3:0xe4
	v_bitop3_b32 v80, v80, s91, v79 bitop3:0xe4
	v_max3_f32 v97, v97, v76, v77
	v_mov_b32_e32 v79, v78
	v_mov_b32_e32 v78, v80
	v_max3_f32 v80, v97, v78, v79
	v_mov_b32_e32 v81, v80
	v_mfma_f32_32x32x16_bf16 v[18:33], v[158:161], v[206:209], v[18:33]
	s_nop 0
	v_permlane32_swap_b32_e32 v80, v81
	v_max_f32_e32 v81, v81, v81
	v_max_f32_e32 v80, v80, v80
	v_max_f32_e32 v80, v80, v81
	v_sub_f32_e32 v81, v80, v192
	v_mul_f32_e32 v81, 0x3db504f3, v81
	v_cmp_ge_f32_e32 vcc, s92, v81
	s_cmp_eq_u64 vcc, exec
	s_cselect_b64 s[2:3], -1, 0
	s_andn2_b64 vcc, exec, s[4:5]
	s_cbranch_vccnz .LBB0_1601
	s_waitcnt vmcnt(0)
	ds_write_b128 v180, v[130:133] offset:16384
	ds_write_b128 v180, v[134:137] offset:24576
	ds_write_b128 v186, v[138:141] offset:49152
	ds_write_b128 v186, v[142:145] offset:57344
